# v80 + P2 role rebalancing: GEMM-first (even) WGs convert only items < 0x8000 of their class, convert-first (odd) WGs also take the partner class items in [0x8000, 0x9c00)
# speedup vs baseline: 1.0213x; 1.0174x over previous
; #define CV_LOAD(c) do { _Pragma("unroll") for (int nh = 0; nh < 2; ++nh) _Pragma("unroll") for (int q = 0; q < 4; ++q) { const float* p_ = (c).src + (size_t)(krow + 4 * q) * (c).N + 32 * nh + 8 * lg; \
;         v[(nh * 4 + q) * 2] = *(const f32x4*)p_; v[(nh * 4 + q) * 2 + 1] = *(const f32x4*)(p_ + 4); } } while (0)
; __device__ __forceinline__ CvItem cv_decode(const void* const* in, unsigned char* ws, int r) {
;     constexpr int I_EI = 32 * 16, I_EO = 8 * 32; CvItem c;
;     if (r < 65 * I_EI) { const int e = r / I_EI, q = r % I_EI, kb = 2 * ((q >> 1) / 16) + (q & 1), nb = (q >> 1) % 16, n0 = 64 * nb, j = n0 & 511, up = n0 >> 9;
;         const float* W = (e < 64) ? (const float*)in[20] + (size_t)e * DM * 1024 : (const float*)in[22];
;         c.src = W + (size_t)(64 * kb) * 1024 + n0; c.N = 1024; c.K = DM; c.scale = SC_WEI;
;         c.dst = ws + WS_WEI + (size_t)e * 1024 * DM + (size_t)((j >> 7) * 256 + up * 128 + (j & 127)) * DM + 64 * kb; }
;     else { r -= 65 * I_EI; const int e = r / I_EO, q = r % I_EO, kb = 2 * ((q >> 1) / 32) + (q & 1), nb = (q >> 1) % 32;
;         const float* W = (e < 64) ? (const float*)in[21] + (size_t)e * EH * DM : (const float*)in[23];
;         c.src = W + (size_t)(64 * kb) * DM + 64 * nb; c.N = DM; c.K = EH; c.scale = SC_WEO;
;         c.dst = ws + WS_WEO + (size_t)e * DM * EH + (size_t)(64 * nb) * EH + 64 * kb; }
;     return c;
; }
; __device__ __forceinline__ void p2_convert_experts(Ctx& F) {
;     const int gw = F.vcu * NWAVES + F.wave, NGW = F.G * NWAVES, lane = F.lane, li = lane & 15, lg = lane >> 4;
;     constexpr int NCV = 65 * (32 * 16 + 8 * 32);
;     int it = gw; CvItem cur; f32x4 v[16];
;     const int krow = 16 * (li >> 2) + (li & 3);
;     ...
;     if (it < NCV) { cur = cv_decode(F.in, F.ws, it); CV_LOAD(cur); }
; __global__ void __launch_bounds__(NWAVES * 64, 2) fwd_kernel(Args args) {
;     ...
;     if (IN(2)) {
;         if (F.vcu & 1) p2_convert_experts(F);
.LBB0_149:
	s_cmp_lt_i32 s86, 3
	s_cselect_b64 s[0:1], -1, 0
	s_cmp_gt_i32 s87, 2
	s_mov_b64 s[12:13], s[52:53]
	s_cselect_b64 s[4:5], -1, 0
	s_mov_b64 s[14:15], s[54:55]
	s_mov_b64 s[16:17], s[56:57]
	s_mov_b64 s[18:19], s[58:59]
	s_mov_b64 s[6:7], s[46:47]
	s_mov_b64 s[10:11], s[50:51]
	s_and_b64 s[0:1], s[0:1], s[4:5]
	v_writelane_b32 v253, s4, 41
	s_andn2_b64 vcc, exec, s[0:1]
	s_nop 0
	v_writelane_b32 v253, s5, 42
	v_writelane_b32 v253, s6, 43
	v_writelane_b32 v253, s7, 44
	v_writelane_b32 v253, s8, 45
	v_writelane_b32 v253, s9, 46
	v_writelane_b32 v253, s10, 47
	v_writelane_b32 v253, s11, 48
	v_writelane_b32 v253, s12, 49
	v_writelane_b32 v253, s13, 50
	v_writelane_b32 v253, s14, 51
	v_writelane_b32 v253, s15, 52
	v_writelane_b32 v253, s16, 53
	v_writelane_b32 v253, s17, 54
	v_writelane_b32 v253, s18, 55
	v_writelane_b32 v253, s19, 56
	s_cbranch_vccnz .LBB0_308
	s_mov_b32 s101, 0
	s_and_b32 s3, s85, 1
	s_cmp_eq_u32 s3, 0
	s_cselect_b64 s[0:1], -1, 0
	s_cmp_eq_u32 s3, 1
	s_cselect_b64 s[4:5], -1, 0
	s_and_b64 vcc, exec, s[4:5]
	s_cbranch_vccz .LBB0_155
	s_lshl_b32 s3, s85, 3
	s_add_i32 s3, s3, s67
.Lcv1_reenter:
	v_and_b32_e32 v194, 15, v0
	s_cmp_gt_i32 s3, 0x9bff
	v_lshlrev_b32_e32 v195, 2, v0
	s_cbranch_scc1 .LBB0_191
	s_cmp_gt_i32 s3, 0x81ff
	s_cbranch_scc0 .LBB0_156
	s_add_i32 s5, s3, 0xffff7e00
	s_lshr_b32 s4, s5, 8
	s_lshr_b32 s6, s3, 5
	v_readlane_b32 s7, v253, 4
	s_and_b32 s6, s6, 6
	s_bfe_u32 s30, s7, 0x10006
	s_lshl_b32 s8, s4, 20
	s_mov_b32 s9, 0
	s_or_b32 s10, s6, s30
	s_lshl_b64 s[6:7], s[8:9], 2
	s_add_u32 s6, s54, s6
	s_addc_u32 s7, s55, s7
	s_cmpk_lt_u32 s5, 0x4000
	s_cselect_b32 s5, s7, s59
	s_cselect_b32 s6, s6, s58
	s_lshl_b32 s8, s10, 6
	s_lshl_b32 s7, s10, 19
	s_add_u32 s6, s6, s7
	s_addc_u32 s5, s5, 0
	s_lshl_b32 s7, s3, 5
	s_and_b32 s10, s7, 0x7c0
	s_lshl_b32 s7, s10, 2
	s_add_u32 s6, s6, s7
	s_addc_u32 s7, s5, 0
	s_mov_b32 s5, s9
	s_lshl_b64 s[4:5], s[4:5], 20
	s_add_u32 s4, s96, s4
	s_addc_u32 s5, s97, s5
	s_lshl_b32 s9, s10, 9
	s_add_u32 s4, s4, s9
	s_addc_u32 s5, s5, 0
	s_add_u32 s4, s4, s8
	s_addc_u32 s5, s5, 0
	s_add_u32 s18, s4, 0x13000000
	s_addc_u32 s19, s5, 0
	s_cbranch_execz .LBB0_157
	s_mov_b32 s24, 4.0
	s_movk_i32 s31, 0x200
	s_mov_b64 s[4:5], 0x800
	s_branch .LBB0_158

; #define CV_LOAD(c) do { _Pragma("unroll") for (int nh = 0; nh < 2; ++nh) _Pragma("unroll") for (int q = 0; q < 4; ++q) { const float* p_ = (c).src + (size_t)(krow + 4 * q) * (c).N + 32 * nh + 8 * lg; \
;         v[(nh * 4 + q) * 2] = *(const f32x4*)p_; v[(nh * 4 + q) * 2 + 1] = *(const f32x4*)(p_ + 4); } } while (0)
; __device__ __forceinline__ void p2_convert_experts(Ctx& F) {
;     const int gw = F.vcu * NWAVES + F.wave, NGW = F.G * NWAVES, lane = F.lane, li = lane & 15, lg = lane >> 4;
;     constexpr int NCV = 65 * (32 * 16 + 8 * 32);
;     int it = gw; CvItem cur; f32x4 v[16];
;     const int krow = 16 * (li >> 2) + (li & 3);
;     ...
;     if (it < NCV) { cur = cv_decode(F.in, F.ws, it); CV_LOAD(cur); }
;     while (it < NCV) {
; __global__ void __launch_bounds__(NWAVES * 64, 2) fwd_kernel(Args args) {
;     ...
;         if (F.vcu & 1) p2_convert_experts(F);
.LBB0_191:
	s_cmp_lg_u32 s101, 0
	s_cbranch_scc1 .Lcv1_done
	s_mov_b32 s101, 1
	s_xor_b32 s3, s85, 1
	s_lshl_b32 s3, s3, 3
	s_add_i32 s3, s3, s67
	s_add_i32 s3, s3, 0x8000
	s_branch .Lcv1_reenter

; #define CV_LOAD(c) do { _Pragma("unroll") for (int nh = 0; nh < 2; ++nh) _Pragma("unroll") for (int q = 0; q < 4; ++q) { const float* p_ = (c).src + (size_t)(krow + 4 * q) * (c).N + 32 * nh + 8 * lg; \
;         v[(nh * 4 + q) * 2] = *(const f32x4*)p_; v[(nh * 4 + q) * 2 + 1] = *(const f32x4*)(p_ + 4); } } while (0)
; __device__ __forceinline__ CvItem cv_decode(const void* const* in, unsigned char* ws, int r) {
;     constexpr int I_EI = 32 * 16, I_EO = 8 * 32; CvItem c;
;     if (r < 65 * I_EI) { const int e = r / I_EI, q = r % I_EI, kb = 2 * ((q >> 1) / 16) + (q & 1), nb = (q >> 1) % 16, n0 = 64 * nb, j = n0 & 511, up = n0 >> 9;
;         const float* W = (e < 64) ? (const float*)in[20] + (size_t)e * DM * 1024 : (const float*)in[22];
;         c.src = W + (size_t)(64 * kb) * 1024 + n0; c.N = 1024; c.K = DM; c.scale = SC_WEI;
;         c.dst = ws + WS_WEI + (size_t)e * 1024 * DM + (size_t)((j >> 7) * 256 + up * 128 + (j & 127)) * DM + 64 * kb; }
;     else { r -= 65 * I_EI; const int e = r / I_EO, q = r % I_EO, kb = 2 * ((q >> 1) / 32) + (q & 1), nb = (q >> 1) % 32;
;         const float* W = (e < 64) ? (const float*)in[21] + (size_t)e * EH * DM : (const float*)in[23];
;         c.src = W + (size_t)(64 * kb) * DM + 64 * nb; c.N = DM; c.K = EH; c.scale = SC_WEO;
;         c.dst = ws + WS_WEO + (size_t)e * DM * EH + (size_t)(64 * nb) * EH + 64 * kb; }
;     return c;
; }
; __device__ __forceinline__ void p2_convert_experts(Ctx& F) {
;     const int gw = F.vcu * NWAVES + F.wave, NGW = F.G * NWAVES, lane = F.lane, li = lane & 15, lg = lane >> 4;
;     constexpr int NCV = 65 * (32 * 16 + 8 * 32);
;     int it = gw; CvItem cur; f32x4 v[16];
;     const int krow = 16 * (li >> 2) + (li & 3);
;     ...
;     if (it < NCV) { cur = cv_decode(F.in, F.ws, it); CV_LOAD(cur); }
; __global__ void __launch_bounds__(NWAVES * 64, 2) fwd_kernel(Args args) {
;     ...
;         if (!(F.vcu & 1)) p2_convert_experts(F);
.LBB0_214:
	s_andn2_b64 vcc, exec, s[0:1]
	s_cbranch_vccnz .LBB0_254
	s_lshl_b32 s0, s85, 3
	s_add_i32 s3, s0, s67
	s_cmp_gt_i32 s3, 0x7fff
	s_cbranch_scc1 .LBB0_254
	s_cmp_gt_i32 s3, 0x81ff
	s_cbranch_scc0 .LBB0_219
	s_add_i32 s1, s3, 0xffff7e00
	s_lshr_b32 s0, s1, 8
	s_lshr_b32 s4, s3, 5
	v_readlane_b32 s5, v253, 4
	s_and_b32 s4, s4, 6
	s_bfe_u32 s28, s5, 0x10006
	s_lshl_b32 s6, s0, 20
	s_mov_b32 s7, 0
	s_or_b32 s8, s4, s28
	s_lshl_b64 s[4:5], s[6:7], 2
	s_add_u32 s4, s54, s4
	s_addc_u32 s5, s55, s5
	s_cmpk_lt_u32 s1, 0x4000
	s_cselect_b32 s1, s5, s59
	s_cselect_b32 s4, s4, s58
	s_lshl_b32 s6, s8, 6
	s_lshl_b32 s5, s8, 19
	s_add_u32 s4, s4, s5
	s_addc_u32 s1, s1, 0
	s_lshl_b32 s5, s3, 5
	s_and_b32 s8, s5, 0x7c0
	s_lshl_b32 s5, s8, 2
	s_add_u32 s4, s4, s5
	s_addc_u32 s5, s1, 0
	s_mov_b32 s1, s7
	s_lshl_b64 s[0:1], s[0:1], 20
	s_add_u32 s0, s96, s0
	s_addc_u32 s1, s97, s1
	s_lshl_b32 s7, s8, 9
	s_add_u32 s0, s0, s7
	s_addc_u32 s1, s1, 0
	s_add_u32 s0, s0, s6
	s_addc_u32 s1, s1, 0
	s_add_u32 s16, s0, 0x13000000
	s_addc_u32 s17, s1, 0
	s_cbranch_execz .LBB0_220
	s_mov_b32 s22, 4.0
	s_movk_i32 s29, 0x200
	s_mov_b64 s[0:1], 0x800
	s_branch .LBB0_221

; __device__ __forceinline__ unsigned pk2c(float lo, float hi) { const bf16x2_t r = __builtin_convertvector((f32x2){lo, hi}, bf16x2_t); return __builtin_bit_cast(unsigned, r); }
; __device__ __forceinline__ CvItem cv_decode(const void* const* in, unsigned char* ws, int r) {
;     constexpr int I_EI = 32 * 16, I_EO = 8 * 32; CvItem c;
;     if (r < 65 * I_EI) { const int e = r / I_EI, q = r % I_EI, kb = 2 * ((q >> 1) / 16) + (q & 1), nb = (q >> 1) % 16, n0 = 64 * nb, j = n0 & 511, up = n0 >> 9;
;         const float* W = (e < 64) ? (const float*)in[20] + (size_t)e * DM * 1024 : (const float*)in[22];
;         c.src = W + (size_t)(64 * kb) * 1024 + n0; c.N = 1024; c.K = DM; c.scale = SC_WEI;
;         c.dst = ws + WS_WEI + (size_t)e * 1024 * DM + (size_t)((j >> 7) * 256 + up * 128 + (j & 127)) * DM + 64 * kb; }
;     else { r -= 65 * I_EI; const int e = r / I_EO, q = r % I_EO, kb = 2 * ((q >> 1) / 32) + (q & 1), nb = (q >> 1) % 32;
;         const float* W = (e < 64) ? (const float*)in[21] + (size_t)e * EH * DM : (const float*)in[23];
;         c.src = W + (size_t)(64 * kb) * DM + 64 * nb; c.N = DM; c.K = EH; c.scale = SC_WEO;
;         c.dst = ws + WS_WEO + (size_t)e * DM * EH + (size_t)(64 * nb) * EH + 64 * kb; }
;     return c;
; }
; __device__ __forceinline__ void p2_convert_experts(Ctx& F) {
;     const int gw = F.vcu * NWAVES + F.wave, NGW = F.G * NWAVES, lane = F.lane, li = lane & 15, lg = lane >> 4;
;     constexpr int NCV = 65 * (32 * 16 + 8 * 32);
;     int it = gw; CvItem cur; f32x4 v[16];
;     const int krow = 16 * (li >> 2) + (li & 3);
;     ...
;     if (it < NCV) { cur = cv_decode(F.in, F.ws, it); CV_LOAD(cur); }
;     while (it < NCV) {
;         bf16x8 a[2][4];
; #pragma unroll
;         for (int nh = 0; nh < 2; ++nh)
; #pragma unroll
;             for (int q = 0; q < 4; ++q) { const f32x4 lo = v[(nh * 4 + q) * 2], hi = v[(nh * 4 + q) * 2 + 1];
;                 const u32x4 pk = (u32x4){pk2c(lo.x, lo.y), pk2c(lo.z, lo.w), pk2c(hi.x, hi.y), pk2c(hi.z, hi.w)}; a[nh][q] = __builtin_bit_cast(bf16x8, pk); }
;         const CvItem me = cur; const int nit = it + NGW;
;         if (nit < NCV) { cur = cv_decode(F.in, F.ws, nit); CV_LOAD(cur); }
.LBB0_225:
	s_add_i32 s3, s3, s30
	s_cmp_gt_i32 s3, 0x7fff
	s_cselect_b64 s[14:15], -1, 0
	s_and_b64 vcc, exec, s[14:15]
	s_cbranch_vccnz .LBB0_232
	s_cmp_gt_i32 s3, 0x81ff
	s_mov_b64 s[20:21], -1
	s_cbranch_scc0 .LBB0_228
	s_add_i32 s13, s3, 0xffff7e00
	s_lshr_b32 s0, s3, 5
	s_lshr_b32 s12, s13, 8
	s_and_b32 s0, s0, 6
	s_or_b32 s20, s0, s28
	s_lshl_b32 s0, s12, 20
	s_lshl_b64 s[18:19], s[0:1], 2
	s_add_u32 s0, s54, s18
	s_addc_u32 s18, s55, s19
	s_cmpk_lt_u32 s13, 0x4000
	s_cselect_b32 s13, s18, s59
	s_cselect_b32 s21, s0, s58
	s_lshl_b32 s0, s20, 6
	s_lshl_b64 s[18:19], s[0:1], 13
	s_add_u32 s18, s21, s18
	s_addc_u32 s13, s13, s19
	s_and_b32 s20, s40, 0x7c0
	s_lshl_b32 s19, s20, 2
	s_add_u32 s18, s18, s19
	s_addc_u32 s19, s13, 0
	s_mov_b32 s13, s1
	s_lshl_b64 s[12:13], s[12:13], 20
	s_add_u32 s12, s33, s12
	s_addc_u32 s13, s34, s13
	s_lshl_b32 s20, s20, 9
	s_add_u32 s12, s12, s20
	s_addc_u32 s13, s13, 0
	s_add_u32 s12, s12, s0
	s_addc_u32 s13, s13, 0
	s_mov_b64 s[20:21], 0
